# speedup vs baseline: 1.0448x; 1.0000x over previous
.Lp_main:
	s_load_dwordx2 s[10:11], s[0:1], 0x0
	s_load_dwordx4 s[12:15], s[0:1], 0x10
	s_load_dwordx2 s[16:17], s[0:1], 0x20
	s_load_dwordx4 s[20:23], s[0:1], 0x28
	v_readfirstlane_b32 s3, v0
	v_and_b32_e32 v154, 63, v0
	v_lshrrev_b32_e32 v155, 5, v154
	v_lshlrev_b32_e32 v156, 4, v0
	v_lshlrev_b32_e32 v157, 4, v154
	v_lshlrev_b32_e32 v158, 8, v1
	v_lshl_add_u32 v158, v155, 5, v158
	v_lshlrev_b32_e32 v159, 4, v155
	v_lshrrev_b32_e32 v160, 3, v0
	v_lshlrev_b32_e32 v160, 12, v160
	v_and_b32_e32 v161, 7, v0
	v_lshl_add_u32 v160, v161, 4, v160
	s_lshr_b32 s41, s2, 3
	s_and_b32 s42, s2, 7
	s_lshl_b32 s24, s42, 2
	s_bfe_u32 s25, s2, 0x20003
	s_add_u32 s24, s24, s25
	s_lshr_b32 s25, s2, 5
	s_lshr_b32 s26, s3, 6
	s_lshl_b32 s27, s25, 2
	s_add_u32 s27, s27, s26
	s_mov_b32 s4, 0x4038aa3b
	s_mov_b32 s5, s4
	s_lshl_b32 s40, s26, 6
	s_waitcnt lgkmcnt(0)
	s_lshl_b32 s28, s24, 15
	s_add_u32 s28, s28, 0x1000
	s_add_u32 s10, s10, s28
	s_addc_u32 s11, s11, 0
	s_lshl_b32 s34, s41, 17
	s_lshl_b32 s35, s42, 9
	s_add_u32 s34, s34, s35
	s_add_u32 s34, s14, s34
	s_addc_u32 s35, s15, 0
	s_lshl_b32 s28, s27, 13
	s_add_u32 s28, s8, s28
	s_addc_u32 s29, s9, 0
	s_lshl_b32 s30, s27, 7
	s_add_u32 s30, s12, s30
	s_addc_u32 s31, s13, 0
	global_load_dwordx4 v[2:5], v156, s[10:11] offset:-4096
	global_load_dwordx4 v[6:9], v156, s[10:11] offset:0
	s_add_u32 s10, s10, 0x2000
	s_addc_u32 s11, s11, 0
	global_load_dwordx4 v[10:13], v156, s[10:11] offset:-4096
	global_load_dwordx4 v[14:17], v156, s[10:11] offset:0
	s_add_u32 s10, s10, 0x2000
	s_addc_u32 s11, s11, 0
	global_load_dwordx4 v[18:21], v156, s[10:11] offset:-4096
	global_load_dwordx4 v[22:25], v156, s[10:11] offset:0
	s_add_u32 s10, s10, 0x2000
	s_addc_u32 s11, s11, 0
	global_load_dwordx4 v[26:29], v156, s[10:11] offset:-4096
	global_load_dwordx4 v[30:33], v156, s[10:11] offset:0
	global_load_dwordx4 v[130:133], v160, s[34:35] offset:0
	global_load_dwordx4 v[134:137], v160, s[34:35] offset:128
	global_load_dwordx4 v[138:141], v160, s[34:35] offset:256
	global_load_dwordx4 v[142:145], v160, s[34:35] offset:384
	global_load_dwordx4 v[34:37], v158, s[28:29] offset:0
	global_load_dwordx4 v[38:41], v158, s[28:29] offset:16
	global_load_dwordx4 v[42:45], v158, s[28:29] offset:64
	global_load_dwordx4 v[46:49], v158, s[28:29] offset:80
	global_load_dwordx4 v[50:53], v158, s[28:29] offset:128
	global_load_dwordx4 v[54:57], v158, s[28:29] offset:144
	global_load_dwordx4 v[58:61], v158, s[28:29] offset:192
	global_load_dwordx4 v[62:65], v158, s[28:29] offset:208
	global_load_dwordx4 v[66:69], v159, s[30:31] offset:0
	global_load_dwordx4 v[70:73], v159, s[30:31] offset:32
	global_load_dwordx4 v[74:77], v159, s[30:31] offset:64
	global_load_dwordx4 v[78:81], v159, s[30:31] offset:96
	v_bfe_u32 v163, v0, 1, 3
	v_mul_u32_u24_e32 v163, 0x210, v163
	v_lshrrev_b32_e32 v164, 4, v0
	v_lshl_add_u32 v163, v164, 4, v163
	v_and_b32_e32 v164, 1, v0
	v_lshl_add_u32 v163, v164, 3, v163
	v_lshrrev_b32_e32 v164, 3, v0
	v_mul_u32_u24_e32 v164, 0x110, v164
	v_lshl_add_u32 v164, v161, 3, v164
	v_add_u32_e32 v164, 0x4200, v164
	v_mul_u32_u24_e32 v165, 0x210, v155
	v_lshl_add_u32 v165, v1, 4, v165
	v_mul_u32_u24_e32 v166, 0x110, v1
	v_lshl_add_u32 v166, v155, 4, v166
	v_add_u32_e32 v166, s40, v166
	v_add_u32_e32 v166, 0x4200, v166
	v_mul_u32_u24_e32 v167, 0x880, v155
	v_lshl_add_u32 v167, v1, 1, v167
	v_add_u32_e32 v167, s40, v167
	v_add_u32_e32 v167, 0x4200, v167
	s_lshl_b32 s32, s24, 18
	s_lshl_b32 s33, s27, 11
	s_add_u32 s32, s32, s33
	s_add_u32 s32, s16, s32
	s_addc_u32 s33, s17, 0
	s_lshl_b32 s36, s41, 16
	s_lshl_b32 s37, s42, 13
	s_add_u32 s36, s36, s37
	s_lshl_b32 s37, s26, 11
	s_add_u32 s36, s36, s37
	s_add_u32 s36, s20, s36
	s_addc_u32 s37, s21, 0
	s_lshl_b32 s38, s42, 18
	s_lshl_b32 s39, s26, 16
	s_add_u32 s38, s38, s39
	s_lshl_b32 s39, s41, 11
	s_add_u32 s38, s38, s39
	s_add_u32 s38, s22, s38
	s_addc_u32 s39, s23, 0
	s_waitcnt vmcnt(23)
	v_cvt_pk_f16_f32 v2, v2, v3
	v_cvt_pk_f16_f32 v3, v4, v5
	ds_write_b64 v163, v[2:3] offset:0
	s_waitcnt vmcnt(22)
	v_cvt_pk_f16_f32 v6, v6, v7
	v_cvt_pk_f16_f32 v7, v8, v9
	ds_write_b64 v163, v[6:7] offset:256
	s_waitcnt vmcnt(21)
	v_cvt_pk_f16_f32 v10, v10, v11
	v_cvt_pk_f16_f32 v11, v12, v13
	ds_write_b64 v163, v[10:11] offset:4224
	s_waitcnt vmcnt(20)
	v_cvt_pk_f16_f32 v14, v14, v15
	v_cvt_pk_f16_f32 v15, v16, v17
	ds_write_b64 v163, v[14:15] offset:4480
	s_waitcnt vmcnt(19)
	v_cvt_pk_f16_f32 v18, v18, v19
	v_cvt_pk_f16_f32 v19, v20, v21
	ds_write_b64 v163, v[18:19] offset:8448
	s_waitcnt vmcnt(18)
	v_cvt_pk_f16_f32 v22, v22, v23
	v_cvt_pk_f16_f32 v23, v24, v25
	ds_write_b64 v163, v[22:23] offset:8704
	s_waitcnt vmcnt(17)
	v_cvt_pk_f16_f32 v26, v26, v27
	v_cvt_pk_f16_f32 v27, v28, v29
	ds_write_b64 v163, v[26:27] offset:12672
	s_waitcnt vmcnt(16)
	v_cvt_pk_f16_f32 v30, v30, v31
	v_cvt_pk_f16_f32 v31, v32, v33
	ds_write_b64 v163, v[30:31] offset:12928
	s_waitcnt vmcnt(15)
	v_cvt_pk_f16_f32 v130, v130, v131
	v_cvt_pk_f16_f32 v131, v132, v133
	ds_write_b64 v164, v[130:131] offset:0
	s_waitcnt vmcnt(14)
	v_cvt_pk_f16_f32 v134, v134, v135
	v_cvt_pk_f16_f32 v135, v136, v137
	ds_write_b64 v164, v[134:135] offset:64
	s_waitcnt vmcnt(13)
	v_cvt_pk_f16_f32 v138, v138, v139
	v_cvt_pk_f16_f32 v139, v140, v141
	ds_write_b64 v164, v[138:139] offset:128
	s_waitcnt vmcnt(12)
	v_cvt_pk_f16_f32 v142, v142, v143
	v_cvt_pk_f16_f32 v143, v144, v145
	ds_write_b64 v164, v[142:143] offset:192
	s_waitcnt lgkmcnt(0)
	s_barrier
	ds_read_b128 v[130:133], v166
	ds_read_b128 v[134:137], v166 offset:32
	ds_read_u16 v138, v167 offset:0
	ds_read_u16 v139, v167 offset:272
	ds_read_u16 v140, v167 offset:544
	ds_read_u16 v141, v167 offset:816
	ds_read_u16 v142, v167 offset:1088
	ds_read_u16 v143, v167 offset:1360
	ds_read_u16 v144, v167 offset:1632
	ds_read_u16 v145, v167 offset:1904
	s_waitcnt vmcnt(4)
	v_cvt_pk_f16_f32 v82, v34, v35
	v_cvt_pk_f16_f32 v83, v36, v37
	v_cvt_pk_f16_f32 v84, v38, v39
	v_cvt_pk_f16_f32 v85, v40, v41
	v_cvt_pk_f16_f32 v86, v42, v43
	v_cvt_pk_f16_f32 v87, v44, v45
	v_cvt_pk_f16_f32 v88, v46, v47
	v_cvt_pk_f16_f32 v89, v48, v49
	v_cvt_pk_f16_f32 v90, v50, v51
	v_cvt_pk_f16_f32 v91, v52, v53
	v_cvt_pk_f16_f32 v92, v54, v55
	v_cvt_pk_f16_f32 v93, v56, v57
	v_cvt_pk_f16_f32 v94, v58, v59
	v_cvt_pk_f16_f32 v95, v60, v61
	v_cvt_pk_f16_f32 v96, v62, v63
	v_cvt_pk_f16_f32 v97, v64, v65
	s_waitcnt vmcnt(0)
	v_pk_mul_f32 v[66:67], v[66:67], s[4:5] op_sel_hi:[1,0]
	v_pk_mul_f32 v[68:69], v[68:69], s[4:5] op_sel_hi:[1,0]
	v_pk_mul_f32 v[70:71], v[70:71], s[4:5] op_sel_hi:[1,0]
	v_pk_mul_f32 v[72:73], v[72:73], s[4:5] op_sel_hi:[1,0]
	v_pk_mul_f32 v[74:75], v[74:75], s[4:5] op_sel_hi:[1,0]
	v_pk_mul_f32 v[76:77], v[76:77], s[4:5] op_sel_hi:[1,0]
	v_pk_mul_f32 v[78:79], v[78:79], s[4:5] op_sel_hi:[1,0]
	v_pk_mul_f32 v[80:81], v[80:81], s[4:5] op_sel_hi:[1,0]
	s_waitcnt lgkmcnt(8)
	global_store_dwordx4 v157, v[130:133], s[36:37] sc1
	global_store_dwordx4 v157, v[134:137], s[36:37] offset:1024 sc1
	s_waitcnt lgkmcnt(0)
	v_lshl_or_b32 v138, v139, 16, v138
	v_lshl_or_b32 v139, v141, 16, v140
	v_lshl_or_b32 v140, v143, 16, v142
	v_lshl_or_b32 v141, v145, 16, v144
	global_store_dwordx4 v157, v[138:141], s[38:39] sc1
	ds_read_u16 v142, v167 offset:4352
	ds_read_u16 v143, v167 offset:4624
	ds_read_u16 v144, v167 offset:4896
	ds_read_u16 v145, v167 offset:5168
	ds_read_u16 v146, v167 offset:5440
	ds_read_u16 v147, v167 offset:5712
	ds_read_u16 v148, v167 offset:5984
	ds_read_u16 v149, v167 offset:6256
	ds_read_b128 v[2:5], v165 offset:0
	ds_read_b128 v[6:9], v165 offset:1056
	ds_read_b128 v[10:13], v165 offset:2112
	ds_read_b128 v[14:17], v165 offset:3168
	s_waitcnt lgkmcnt(4)
	v_lshl_or_b32 v142, v143, 16, v142
	v_lshl_or_b32 v143, v145, 16, v144
	v_lshl_or_b32 v144, v147, 16, v146
	v_lshl_or_b32 v145, v149, 16, v148
	global_store_dwordx4 v157, v[142:145], s[38:39] offset:1024 sc1
	ds_read_b128 v[18:21], v165 offset:4224
	ds_read_b128 v[22:25], v165 offset:5280
	ds_read_b128 v[26:29], v165 offset:6336
	ds_read_b128 v[30:33], v165 offset:7392
	ds_read_b128 v[34:37], v165 offset:8448
	ds_read_b128 v[38:41], v165 offset:9504
	ds_read_b128 v[42:45], v165 offset:10560
	ds_read_b128 v[46:49], v165 offset:11616
	s_waitcnt lgkmcnt(8)
	v_mfma_f32_32x32x16_f16 v[98:113], v[82:85], v[2:5], 0
	v_mfma_f32_32x32x16_f16 v[98:113], v[86:89], v[6:9], v[98:113]
	v_mfma_f32_32x32x16_f16 v[98:113], v[90:93], v[10:13], v[98:113]
	v_mfma_f32_32x32x16_f16 v[98:113], v[94:97], v[14:17], v[98:113]
	ds_read_b128 v[50:53], v165 offset:12672
	ds_read_b128 v[54:57], v165 offset:13728
	ds_read_b128 v[58:61], v165 offset:14784
	ds_read_b128 v[62:65], v165 offset:15840
	s_waitcnt lgkmcnt(8)
	v_mfma_f32_32x32x16_f16 v[114:129], v[82:85], v[18:21], 0
	v_mfma_f32_32x32x16_f16 v[114:129], v[86:89], v[22:25], v[114:129]
	v_mfma_f32_32x32x16_f16 v[114:129], v[90:93], v[26:29], v[114:129]
	v_mfma_f32_32x32x16_f16 v[114:129], v[94:97], v[30:33], v[114:129]
	s_nop 7
	v_pk_fma_f32 v[130:131], v[98:99], s[4:5], v[66:67] op_sel_hi:[1,0,1]
	v_pk_fma_f32 v[132:133], v[100:101], s[4:5], v[68:69] op_sel_hi:[1,0,1]
	v_pk_fma_f32 v[134:135], v[102:103], s[4:5], v[70:71] op_sel_hi:[1,0,1]
	v_pk_fma_f32 v[136:137], v[104:105], s[4:5], v[72:73] op_sel_hi:[1,0,1]
	v_pk_fma_f32 v[138:139], v[106:107], s[4:5], v[74:75] op_sel_hi:[1,0,1]
	v_pk_fma_f32 v[140:141], v[108:109], s[4:5], v[76:77] op_sel_hi:[1,0,1]
	v_pk_fma_f32 v[142:143], v[110:111], s[4:5], v[78:79] op_sel_hi:[1,0,1]
	v_pk_fma_f32 v[144:145], v[112:113], s[4:5], v[80:81] op_sel_hi:[1,0,1]
	v_exp_f32_e32 v130, v130
	v_exp_f32_e32 v131, v131
	v_exp_f32_e32 v132, v132
	v_exp_f32_e32 v133, v133
	v_exp_f32_e32 v134, v134
	v_exp_f32_e32 v135, v135
	v_exp_f32_e32 v136, v136
	v_exp_f32_e32 v137, v137
	v_exp_f32_e32 v138, v138
	v_exp_f32_e32 v139, v139
	v_exp_f32_e32 v140, v140
	v_exp_f32_e32 v141, v141
	v_exp_f32_e32 v142, v142
	v_exp_f32_e32 v143, v143
	v_exp_f32_e32 v144, v144
	v_exp_f32_e32 v145, v145
	v_pk_add_f32 v[130:131], v[130:131], 1.0 op_sel_hi:[1,0]
	v_pk_add_f32 v[132:133], v[132:133], 1.0 op_sel_hi:[1,0]
	v_pk_add_f32 v[134:135], v[134:135], 1.0 op_sel_hi:[1,0]
	v_pk_add_f32 v[136:137], v[136:137], 1.0 op_sel_hi:[1,0]
	v_pk_add_f32 v[138:139], v[138:139], 1.0 op_sel_hi:[1,0]
	v_pk_add_f32 v[140:141], v[140:141], 1.0 op_sel_hi:[1,0]
	v_pk_add_f32 v[142:143], v[142:143], 1.0 op_sel_hi:[1,0]
	v_pk_add_f32 v[144:145], v[144:145], 1.0 op_sel_hi:[1,0]
	v_rcp_f32_e32 v130, v130
	v_rcp_f32_e32 v131, v131
	v_rcp_f32_e32 v132, v132
	v_rcp_f32_e32 v133, v133
	v_rcp_f32_e32 v134, v134
	v_rcp_f32_e32 v135, v135
	v_rcp_f32_e32 v136, v136
	v_rcp_f32_e32 v137, v137
	v_rcp_f32_e32 v138, v138
	v_rcp_f32_e32 v139, v139
	v_rcp_f32_e32 v140, v140
	v_rcp_f32_e32 v141, v141
	v_rcp_f32_e32 v142, v142
	v_rcp_f32_e32 v143, v143
	v_rcp_f32_e32 v144, v144
	v_rcp_f32_e32 v145, v145
	v_pk_fma_f32 v[130:131], v[130:131], 2.0, 1.0 op_sel_hi:[1,0,0] neg_lo:[1,0,0] neg_hi:[1,0,0]
	v_pk_fma_f32 v[132:133], v[132:133], 2.0, 1.0 op_sel_hi:[1,0,0] neg_lo:[1,0,0] neg_hi:[1,0,0]
	v_pk_fma_f32 v[134:135], v[134:135], 2.0, 1.0 op_sel_hi:[1,0,0] neg_lo:[1,0,0] neg_hi:[1,0,0]
	v_pk_fma_f32 v[136:137], v[136:137], 2.0, 1.0 op_sel_hi:[1,0,0] neg_lo:[1,0,0] neg_hi:[1,0,0]
	v_pk_fma_f32 v[138:139], v[138:139], 2.0, 1.0 op_sel_hi:[1,0,0] neg_lo:[1,0,0] neg_hi:[1,0,0]
	v_pk_fma_f32 v[140:141], v[140:141], 2.0, 1.0 op_sel_hi:[1,0,0] neg_lo:[1,0,0] neg_hi:[1,0,0]
	v_pk_fma_f32 v[142:143], v[142:143], 2.0, 1.0 op_sel_hi:[1,0,0] neg_lo:[1,0,0] neg_hi:[1,0,0]
	v_pk_fma_f32 v[144:145], v[144:145], 2.0, 1.0 op_sel_hi:[1,0,0] neg_lo:[1,0,0] neg_hi:[1,0,0]
	v_cvt_pk_f16_f32 v146, v130, v131
	v_cvt_pk_f16_f32 v147, v132, v133
	v_cvt_pk_f16_f32 v148, v134, v135
	v_cvt_pk_f16_f32 v149, v136, v137
	v_cvt_pk_f16_f32 v150, v138, v139
	v_cvt_pk_f16_f32 v151, v140, v141
	v_cvt_pk_f16_f32 v152, v142, v143
	v_cvt_pk_f16_f32 v153, v144, v145
	s_nop 1
	v_permlane32_swap_b32_e32 v146, v148
	v_permlane32_swap_b32_e32 v147, v149
	v_permlane32_swap_b32_e32 v150, v152
	v_permlane32_swap_b32_e32 v151, v153
	global_store_dwordx4 v157, v[146:149], s[32:33] sc1
	global_store_dwordx4 v157, v[150:153], s[32:33] offset:1024 sc1
	s_add_u32 s32, s32, 0x10000
	s_addc_u32 s33, s33, 0
	s_waitcnt lgkmcnt(4)
	v_mfma_f32_32x32x16_f16 v[98:113], v[82:85], v[34:37], 0
	v_mfma_f32_32x32x16_f16 v[98:113], v[86:89], v[38:41], v[98:113]
	v_mfma_f32_32x32x16_f16 v[98:113], v[90:93], v[42:45], v[98:113]
	v_mfma_f32_32x32x16_f16 v[98:113], v[94:97], v[46:49], v[98:113]
	v_pk_fma_f32 v[130:131], v[114:115], s[4:5], v[66:67] op_sel_hi:[1,0,1]
	v_pk_fma_f32 v[132:133], v[116:117], s[4:5], v[68:69] op_sel_hi:[1,0,1]
	v_pk_fma_f32 v[134:135], v[118:119], s[4:5], v[70:71] op_sel_hi:[1,0,1]
	v_pk_fma_f32 v[136:137], v[120:121], s[4:5], v[72:73] op_sel_hi:[1,0,1]
	v_pk_fma_f32 v[138:139], v[122:123], s[4:5], v[74:75] op_sel_hi:[1,0,1]
	v_pk_fma_f32 v[140:141], v[124:125], s[4:5], v[76:77] op_sel_hi:[1,0,1]
	v_pk_fma_f32 v[142:143], v[126:127], s[4:5], v[78:79] op_sel_hi:[1,0,1]
	v_pk_fma_f32 v[144:145], v[128:129], s[4:5], v[80:81] op_sel_hi:[1,0,1]
	v_exp_f32_e32 v130, v130
	v_exp_f32_e32 v131, v131
	v_exp_f32_e32 v132, v132
	v_exp_f32_e32 v133, v133
	v_exp_f32_e32 v134, v134
	v_exp_f32_e32 v135, v135
	v_exp_f32_e32 v136, v136
	v_exp_f32_e32 v137, v137
	v_exp_f32_e32 v138, v138
	v_exp_f32_e32 v139, v139
	v_exp_f32_e32 v140, v140
	v_exp_f32_e32 v141, v141
	v_exp_f32_e32 v142, v142
	v_exp_f32_e32 v143, v143
	v_exp_f32_e32 v144, v144
	v_exp_f32_e32 v145, v145
	v_pk_add_f32 v[130:131], v[130:131], 1.0 op_sel_hi:[1,0]
	v_pk_add_f32 v[132:133], v[132:133], 1.0 op_sel_hi:[1,0]
	v_pk_add_f32 v[134:135], v[134:135], 1.0 op_sel_hi:[1,0]
	v_pk_add_f32 v[136:137], v[136:137], 1.0 op_sel_hi:[1,0]
	v_pk_add_f32 v[138:139], v[138:139], 1.0 op_sel_hi:[1,0]
	v_pk_add_f32 v[140:141], v[140:141], 1.0 op_sel_hi:[1,0]
	v_pk_add_f32 v[142:143], v[142:143], 1.0 op_sel_hi:[1,0]
	v_pk_add_f32 v[144:145], v[144:145], 1.0 op_sel_hi:[1,0]
	v_rcp_f32_e32 v130, v130
	v_rcp_f32_e32 v131, v131
	v_rcp_f32_e32 v132, v132
	v_rcp_f32_e32 v133, v133
	v_rcp_f32_e32 v134, v134
	v_rcp_f32_e32 v135, v135
	v_rcp_f32_e32 v136, v136
	v_rcp_f32_e32 v137, v137
	v_rcp_f32_e32 v138, v138
	v_rcp_f32_e32 v139, v139
	v_rcp_f32_e32 v140, v140
	v_rcp_f32_e32 v141, v141
	v_rcp_f32_e32 v142, v142
	v_rcp_f32_e32 v143, v143
	v_rcp_f32_e32 v144, v144
	v_rcp_f32_e32 v145, v145
	v_pk_fma_f32 v[130:131], v[130:131], 2.0, 1.0 op_sel_hi:[1,0,0] neg_lo:[1,0,0] neg_hi:[1,0,0]
	v_pk_fma_f32 v[132:133], v[132:133], 2.0, 1.0 op_sel_hi:[1,0,0] neg_lo:[1,0,0] neg_hi:[1,0,0]
	v_pk_fma_f32 v[134:135], v[134:135], 2.0, 1.0 op_sel_hi:[1,0,0] neg_lo:[1,0,0] neg_hi:[1,0,0]
	v_pk_fma_f32 v[136:137], v[136:137], 2.0, 1.0 op_sel_hi:[1,0,0] neg_lo:[1,0,0] neg_hi:[1,0,0]
	v_pk_fma_f32 v[138:139], v[138:139], 2.0, 1.0 op_sel_hi:[1,0,0] neg_lo:[1,0,0] neg_hi:[1,0,0]
	v_pk_fma_f32 v[140:141], v[140:141], 2.0, 1.0 op_sel_hi:[1,0,0] neg_lo:[1,0,0] neg_hi:[1,0,0]
	v_pk_fma_f32 v[142:143], v[142:143], 2.0, 1.0 op_sel_hi:[1,0,0] neg_lo:[1,0,0] neg_hi:[1,0,0]
	v_pk_fma_f32 v[144:145], v[144:145], 2.0, 1.0 op_sel_hi:[1,0,0] neg_lo:[1,0,0] neg_hi:[1,0,0]
	v_cvt_pk_f16_f32 v146, v130, v131
	v_cvt_pk_f16_f32 v147, v132, v133
	v_cvt_pk_f16_f32 v148, v134, v135
	v_cvt_pk_f16_f32 v149, v136, v137
	v_cvt_pk_f16_f32 v150, v138, v139
	v_cvt_pk_f16_f32 v151, v140, v141
	v_cvt_pk_f16_f32 v152, v142, v143
	v_cvt_pk_f16_f32 v153, v144, v145
	s_nop 1
	v_permlane32_swap_b32_e32 v146, v148
	v_permlane32_swap_b32_e32 v147, v149
	v_permlane32_swap_b32_e32 v150, v152
	v_permlane32_swap_b32_e32 v151, v153
	global_store_dwordx4 v157, v[146:149], s[32:33] sc1
	global_store_dwordx4 v157, v[150:153], s[32:33] offset:1024 sc1
	s_add_u32 s32, s32, 0x10000
	s_addc_u32 s33, s33, 0
	s_waitcnt lgkmcnt(0)
	v_mfma_f32_32x32x16_f16 v[114:129], v[82:85], v[50:53], 0
	v_mfma_f32_32x32x16_f16 v[114:129], v[86:89], v[54:57], v[114:129]
	v_mfma_f32_32x32x16_f16 v[114:129], v[90:93], v[58:61], v[114:129]
	v_mfma_f32_32x32x16_f16 v[114:129], v[94:97], v[62:65], v[114:129]
	v_pk_fma_f32 v[130:131], v[98:99], s[4:5], v[66:67] op_sel_hi:[1,0,1]
	v_pk_fma_f32 v[132:133], v[100:101], s[4:5], v[68:69] op_sel_hi:[1,0,1]
	v_pk_fma_f32 v[134:135], v[102:103], s[4:5], v[70:71] op_sel_hi:[1,0,1]
	v_pk_fma_f32 v[136:137], v[104:105], s[4:5], v[72:73] op_sel_hi:[1,0,1]
	v_pk_fma_f32 v[138:139], v[106:107], s[4:5], v[74:75] op_sel_hi:[1,0,1]
	v_pk_fma_f32 v[140:141], v[108:109], s[4:5], v[76:77] op_sel_hi:[1,0,1]
	v_pk_fma_f32 v[142:143], v[110:111], s[4:5], v[78:79] op_sel_hi:[1,0,1]
	v_pk_fma_f32 v[144:145], v[112:113], s[4:5], v[80:81] op_sel_hi:[1,0,1]
	v_exp_f32_e32 v130, v130
	v_exp_f32_e32 v131, v131
	v_exp_f32_e32 v132, v132
	v_exp_f32_e32 v133, v133
	v_exp_f32_e32 v134, v134
	v_exp_f32_e32 v135, v135
	v_exp_f32_e32 v136, v136
	v_exp_f32_e32 v137, v137
	v_exp_f32_e32 v138, v138
	v_exp_f32_e32 v139, v139
	v_exp_f32_e32 v140, v140
	v_exp_f32_e32 v141, v141
	v_exp_f32_e32 v142, v142
	v_exp_f32_e32 v143, v143
	v_exp_f32_e32 v144, v144
	v_exp_f32_e32 v145, v145
	v_pk_add_f32 v[130:131], v[130:131], 1.0 op_sel_hi:[1,0]
	v_pk_add_f32 v[132:133], v[132:133], 1.0 op_sel_hi:[1,0]
	v_pk_add_f32 v[134:135], v[134:135], 1.0 op_sel_hi:[1,0]
	v_pk_add_f32 v[136:137], v[136:137], 1.0 op_sel_hi:[1,0]
	v_pk_add_f32 v[138:139], v[138:139], 1.0 op_sel_hi:[1,0]
	v_pk_add_f32 v[140:141], v[140:141], 1.0 op_sel_hi:[1,0]
	v_pk_add_f32 v[142:143], v[142:143], 1.0 op_sel_hi:[1,0]
	v_pk_add_f32 v[144:145], v[144:145], 1.0 op_sel_hi:[1,0]
	v_rcp_f32_e32 v130, v130
	v_rcp_f32_e32 v131, v131
	v_rcp_f32_e32 v132, v132
	v_rcp_f32_e32 v133, v133
	v_rcp_f32_e32 v134, v134
	v_rcp_f32_e32 v135, v135
	v_rcp_f32_e32 v136, v136
	v_rcp_f32_e32 v137, v137
	v_rcp_f32_e32 v138, v138
	v_rcp_f32_e32 v139, v139
	v_rcp_f32_e32 v140, v140
	v_rcp_f32_e32 v141, v141
	v_rcp_f32_e32 v142, v142
	v_rcp_f32_e32 v143, v143
	v_rcp_f32_e32 v144, v144
	v_rcp_f32_e32 v145, v145
	v_pk_fma_f32 v[130:131], v[130:131], 2.0, 1.0 op_sel_hi:[1,0,0] neg_lo:[1,0,0] neg_hi:[1,0,0]
	v_pk_fma_f32 v[132:133], v[132:133], 2.0, 1.0 op_sel_hi:[1,0,0] neg_lo:[1,0,0] neg_hi:[1,0,0]
	v_pk_fma_f32 v[134:135], v[134:135], 2.0, 1.0 op_sel_hi:[1,0,0] neg_lo:[1,0,0] neg_hi:[1,0,0]
	v_pk_fma_f32 v[136:137], v[136:137], 2.0, 1.0 op_sel_hi:[1,0,0] neg_lo:[1,0,0] neg_hi:[1,0,0]
	v_pk_fma_f32 v[138:139], v[138:139], 2.0, 1.0 op_sel_hi:[1,0,0] neg_lo:[1,0,0] neg_hi:[1,0,0]
	v_pk_fma_f32 v[140:141], v[140:141], 2.0, 1.0 op_sel_hi:[1,0,0] neg_lo:[1,0,0] neg_hi:[1,0,0]
	v_pk_fma_f32 v[142:143], v[142:143], 2.0, 1.0 op_sel_hi:[1,0,0] neg_lo:[1,0,0] neg_hi:[1,0,0]
	v_pk_fma_f32 v[144:145], v[144:145], 2.0, 1.0 op_sel_hi:[1,0,0] neg_lo:[1,0,0] neg_hi:[1,0,0]
	v_cvt_pk_f16_f32 v146, v130, v131
	v_cvt_pk_f16_f32 v147, v132, v133
	v_cvt_pk_f16_f32 v148, v134, v135
	v_cvt_pk_f16_f32 v149, v136, v137
	v_cvt_pk_f16_f32 v150, v138, v139
	v_cvt_pk_f16_f32 v151, v140, v141
	v_cvt_pk_f16_f32 v152, v142, v143
	v_cvt_pk_f16_f32 v153, v144, v145
	s_nop 1
	v_permlane32_swap_b32_e32 v146, v148
	v_permlane32_swap_b32_e32 v147, v149
	v_permlane32_swap_b32_e32 v150, v152
	v_permlane32_swap_b32_e32 v151, v153
	global_store_dwordx4 v157, v[146:149], s[32:33] sc1
	global_store_dwordx4 v157, v[150:153], s[32:33] offset:1024 sc1
	s_add_u32 s32, s32, 0x10000
	s_addc_u32 s33, s33, 0
	s_nop 7
	v_pk_fma_f32 v[130:131], v[114:115], s[4:5], v[66:67] op_sel_hi:[1,0,1]
	v_pk_fma_f32 v[132:133], v[116:117], s[4:5], v[68:69] op_sel_hi:[1,0,1]
	v_pk_fma_f32 v[134:135], v[118:119], s[4:5], v[70:71] op_sel_hi:[1,0,1]
	v_pk_fma_f32 v[136:137], v[120:121], s[4:5], v[72:73] op_sel_hi:[1,0,1]
	v_pk_fma_f32 v[138:139], v[122:123], s[4:5], v[74:75] op_sel_hi:[1,0,1]
	v_pk_fma_f32 v[140:141], v[124:125], s[4:5], v[76:77] op_sel_hi:[1,0,1]
	v_pk_fma_f32 v[142:143], v[126:127], s[4:5], v[78:79] op_sel_hi:[1,0,1]
	v_pk_fma_f32 v[144:145], v[128:129], s[4:5], v[80:81] op_sel_hi:[1,0,1]
	v_exp_f32_e32 v130, v130
	v_exp_f32_e32 v131, v131
	v_exp_f32_e32 v132, v132
	v_exp_f32_e32 v133, v133
	v_exp_f32_e32 v134, v134
	v_exp_f32_e32 v135, v135
	v_exp_f32_e32 v136, v136
	v_exp_f32_e32 v137, v137
	v_exp_f32_e32 v138, v138
	v_exp_f32_e32 v139, v139
	v_exp_f32_e32 v140, v140
	v_exp_f32_e32 v141, v141
	v_exp_f32_e32 v142, v142
	v_exp_f32_e32 v143, v143
	v_exp_f32_e32 v144, v144
	v_exp_f32_e32 v145, v145
	v_pk_add_f32 v[130:131], v[130:131], 1.0 op_sel_hi:[1,0]
	v_pk_add_f32 v[132:133], v[132:133], 1.0 op_sel_hi:[1,0]
	v_pk_add_f32 v[134:135], v[134:135], 1.0 op_sel_hi:[1,0]
	v_pk_add_f32 v[136:137], v[136:137], 1.0 op_sel_hi:[1,0]
	v_pk_add_f32 v[138:139], v[138:139], 1.0 op_sel_hi:[1,0]
	v_pk_add_f32 v[140:141], v[140:141], 1.0 op_sel_hi:[1,0]
	v_pk_add_f32 v[142:143], v[142:143], 1.0 op_sel_hi:[1,0]
	v_pk_add_f32 v[144:145], v[144:145], 1.0 op_sel_hi:[1,0]
	v_rcp_f32_e32 v130, v130
	v_rcp_f32_e32 v131, v131
	v_rcp_f32_e32 v132, v132
	v_rcp_f32_e32 v133, v133
	v_rcp_f32_e32 v134, v134
	v_rcp_f32_e32 v135, v135
	v_rcp_f32_e32 v136, v136
	v_rcp_f32_e32 v137, v137
	v_rcp_f32_e32 v138, v138
	v_rcp_f32_e32 v139, v139
	v_rcp_f32_e32 v140, v140
	v_rcp_f32_e32 v141, v141
	v_rcp_f32_e32 v142, v142
	v_rcp_f32_e32 v143, v143
	v_rcp_f32_e32 v144, v144
	v_rcp_f32_e32 v145, v145
	v_pk_fma_f32 v[130:131], v[130:131], 2.0, 1.0 op_sel_hi:[1,0,0] neg_lo:[1,0,0] neg_hi:[1,0,0]
	v_pk_fma_f32 v[132:133], v[132:133], 2.0, 1.0 op_sel_hi:[1,0,0] neg_lo:[1,0,0] neg_hi:[1,0,0]
	v_pk_fma_f32 v[134:135], v[134:135], 2.0, 1.0 op_sel_hi:[1,0,0] neg_lo:[1,0,0] neg_hi:[1,0,0]
	v_pk_fma_f32 v[136:137], v[136:137], 2.0, 1.0 op_sel_hi:[1,0,0] neg_lo:[1,0,0] neg_hi:[1,0,0]
	v_pk_fma_f32 v[138:139], v[138:139], 2.0, 1.0 op_sel_hi:[1,0,0] neg_lo:[1,0,0] neg_hi:[1,0,0]
	v_pk_fma_f32 v[140:141], v[140:141], 2.0, 1.0 op_sel_hi:[1,0,0] neg_lo:[1,0,0] neg_hi:[1,0,0]
	v_pk_fma_f32 v[142:143], v[142:143], 2.0, 1.0 op_sel_hi:[1,0,0] neg_lo:[1,0,0] neg_hi:[1,0,0]
	v_pk_fma_f32 v[144:145], v[144:145], 2.0, 1.0 op_sel_hi:[1,0,0] neg_lo:[1,0,0] neg_hi:[1,0,0]
	v_cvt_pk_f16_f32 v146, v130, v131
	v_cvt_pk_f16_f32 v147, v132, v133
	v_cvt_pk_f16_f32 v148, v134, v135
	v_cvt_pk_f16_f32 v149, v136, v137
	v_cvt_pk_f16_f32 v150, v138, v139
	v_cvt_pk_f16_f32 v151, v140, v141
	v_cvt_pk_f16_f32 v152, v142, v143
	v_cvt_pk_f16_f32 v153, v144, v145
	s_nop 1
	v_permlane32_swap_b32_e32 v146, v148
	v_permlane32_swap_b32_e32 v147, v149
	v_permlane32_swap_b32_e32 v150, v152
	v_permlane32_swap_b32_e32 v151, v153
	global_store_dwordx4 v157, v[146:149], s[32:33] sc1
	global_store_dwordx4 v157, v[150:153], s[32:33] offset:1024 sc1
	s_endpgm
